# MFMA/LDS interleave in ml_out: the two 17-MFMA P.V sections per key tile software-pipelined (4-slot fragment ring in dead registers, first three fragments requested before the q.k section); on top of
# baseline (speedup 1.0000x reference)
.LBB0_722:
	s_waitcnt lgkmcnt(0)
	s_barrier
	s_cmp_gt_i32 s74, s73
	v_add_u32_e32 v7, s74, v222
	v_add_u32_e32 v8, 0x400, v130
	s_cbranch_scc1 .LBB0_724
	ds_read_b64_tr_b16 v[140:141], v202
	ds_read_b64_tr_b16 v[142:143], v202 offset:2240
	ds_read_b64_tr_b16 v[144:145], v202 offset:32
	ds_read_b64_tr_b16 v[146:147], v202 offset:2272
	ds_read_b64_tr_b16 v[148:149], v202 offset:64
	ds_read_b64_tr_b16 v[150:151], v202 offset:2304
	ds_read_b128 v[122:125], v235
	ds_read_b128 v[136:139], v235 offset:64
	ds_read_b128 v[132:135], v235 offset:4352
	v_cmp_le_i32_e32 vcc, v7, v126
	s_waitcnt lgkmcnt(2)
	v_mfma_f32_16x16x32_bf16 v[122:125], v[10:13], v[122:125], 0
	s_waitcnt lgkmcnt(1)
	v_mfma_f32_16x16x32_bf16 v[122:125], v[14:17], v[136:139], v[122:125]
	ds_read_b128 v[136:139], v235 offset:4416
	s_waitcnt lgkmcnt(1)
	v_mfma_f32_16x16x32_bf16 v[132:135], v[10:13], v[132:135], 0
	s_waitcnt lgkmcnt(0)
	v_mfma_f32_16x16x32_bf16 v[132:135], v[14:17], v[136:139], v[132:135]
	ds_read_b128 v[136:139], v235 offset:128
	s_waitcnt lgkmcnt(0)
	v_mfma_f32_16x16x32_bf16 v[122:125], v[18:21], v[136:139], v[122:125]
	ds_read_b128 v[136:139], v235 offset:4480
	s_waitcnt lgkmcnt(0)
	v_mfma_f32_16x16x32_bf16 v[132:135], v[18:21], v[136:139], v[132:135]
	ds_read_b128 v[136:139], v235 offset:192
	s_waitcnt lgkmcnt(0)
	v_mfma_f32_16x16x32_bf16 v[136:139], v[22:25], v[136:139], v[122:125]
	s_nop 2
	ds_read_b128 v[122:125], v235 offset:4544
	s_waitcnt lgkmcnt(0)
	v_mfma_f32_16x16x32_bf16 v[122:125], v[22:25], v[122:125], v[132:135]
	s_nop 2
	ds_read2_b32 v[132:133], v8 offset1:16
	ds_read2_b32 v[134:135], v130 offset1:16
	s_waitcnt lgkmcnt(0)
	v_sub_f32_e32 v9, v132, v134
	v_add_f32_e32 v131, v26, v9
	v_mul_f32_e32 v131, 0x3fb8aa3b, v131
	v_exp_f32_e32 v131, v131
	s_nop 0
	v_cndmask_b32_e32 v131, 0, v131, vcc
	v_mul_f32_e32 v131, v136, v131
	v_bfe_u32 v132, v131, 16, 1
	v_add3_u32 v131, v131, v132, s14
	ds_write_b16_d16_hi v236, v131
	v_add_f32_e32 v131, v27, v9
	v_mul_f32_e32 v131, 0x3fb8aa3b, v131
	v_exp_f32_e32 v131, v131
	v_cmp_le_i32_e32 vcc, v7, v127
	s_nop 1
	v_cndmask_b32_e32 v131, 0, v131, vcc
	v_mul_f32_e32 v131, v137, v131
	v_bfe_u32 v132, v131, 16, 1
	v_add3_u32 v131, v131, v132, s14
	ds_write_b16_d16_hi v236, v131 offset:80
	v_add_f32_e32 v131, v28, v9
	v_mul_f32_e32 v131, 0x3fb8aa3b, v131
	v_exp_f32_e32 v131, v131
	v_add_f32_e32 v9, v29, v9
	v_mul_f32_e32 v9, 0x3fb8aa3b, v9
	v_exp_f32_e32 v9, v9
	v_cmp_le_i32_e32 vcc, v7, v128
	s_nop 1
	v_cndmask_b32_e32 v131, 0, v131, vcc
	v_mul_f32_e32 v131, v138, v131
	v_cmp_le_i32_e32 vcc, v7, v129
	v_bfe_u32 v132, v131, 16, 1
	v_add3_u32 v131, v131, v132, s14
	v_cndmask_b32_e32 v9, 0, v9, vcc
	v_mul_f32_e32 v9, v139, v9
	ds_write_b16_d16_hi v236, v131 offset:160
	v_bfe_u32 v131, v9, 16, 1
	v_add3_u32 v9, v9, v131, s14
	v_sub_f32_e32 v131, v133, v135
	v_add_f32_e32 v132, v26, v131
	v_mul_f32_e32 v132, 0x3fb8aa3b, v132
	v_exp_f32_e32 v132, v132
	ds_write_b16_d16_hi v236, v9 offset:240
	v_add_u32_e32 v9, 16, v7
	v_cmp_le_i32_e32 vcc, v9, v126
	s_nop 1
	v_cndmask_b32_e32 v132, 0, v132, vcc
	v_mul_f32_e32 v122, v122, v132
	v_bfe_u32 v132, v122, 16, 1
	v_add3_u32 v122, v122, v132, s14
	ds_write_b16_d16_hi v236, v122 offset:32
	v_add_f32_e32 v122, v27, v131
	v_mul_f32_e32 v122, 0x3fb8aa3b, v122
	v_exp_f32_e32 v122, v122
	v_cmp_le_i32_e32 vcc, v9, v127
	s_nop 1
	v_cndmask_b32_e32 v122, 0, v122, vcc
	v_mul_f32_e32 v122, v123, v122
	v_bfe_u32 v123, v122, 16, 1
	v_add3_u32 v122, v122, v123, s14
	ds_write_b16_d16_hi v236, v122 offset:112
	v_add_f32_e32 v122, v28, v131
	v_mul_f32_e32 v122, 0x3fb8aa3b, v122
	v_exp_f32_e32 v122, v122
	v_cmp_le_i32_e32 vcc, v9, v128
	s_nop 1
	v_cndmask_b32_e32 v122, 0, v122, vcc
	v_mul_f32_e32 v122, v124, v122
	v_bfe_u32 v123, v122, 16, 1
	v_add3_u32 v122, v122, v123, s14
	ds_write_b16_d16_hi v236, v122 offset:192
	v_add_f32_e32 v122, v29, v131
	v_mul_f32_e32 v122, 0x3fb8aa3b, v122
	v_exp_f32_e32 v122, v122
	v_cmp_le_i32_e32 vcc, v9, v129
	s_nop 1
	v_cndmask_b32_e32 v9, 0, v122, vcc
	v_mul_f32_e32 v9, v125, v9
	v_bfe_u32 v122, v9, 16, 1
	v_add3_u32 v9, v9, v122, s14
	ds_write_b16_d16_hi v236, v9 offset:272
	ds_read_b128 v[122:125], v237
	ds_read_b64_tr_b16 v[152:153], v202 offset:96
	ds_read_b64_tr_b16 v[154:155], v202 offset:2336
	s_waitcnt lgkmcnt(2)
	v_mfma_f32_16x16x32_bf16 v[54:57], v[122:125], v[140:143], v[54:57]
	ds_read_b64_tr_b16 v[140:141], v202 offset:128
	ds_read_b64_tr_b16 v[142:143], v202 offset:2368
	v_mfma_f32_16x16x32_bf16 v[62:65], v[122:125], v[144:147], v[62:65]
	ds_read_b64_tr_b16 v[144:145], v202 offset:160
	ds_read_b64_tr_b16 v[146:147], v202 offset:2400
	v_mfma_f32_16x16x32_bf16 v[58:61], v[122:125], v[148:151], v[58:61]
	ds_read_b64_tr_b16 v[148:149], v202 offset:192
	ds_read_b64_tr_b16 v[150:151], v202 offset:2432
	s_waitcnt lgkmcnt(6)
	v_mfma_f32_16x16x32_bf16 v[74:77], v[122:125], v[152:155], v[74:77]
	ds_read_b64_tr_b16 v[152:153], v202 offset:224
	ds_read_b64_tr_b16 v[154:155], v202 offset:2464
	s_waitcnt lgkmcnt(6)
	v_mfma_f32_16x16x32_bf16 v[70:73], v[122:125], v[140:143], v[70:73]
	ds_read_b64_tr_b16 v[140:141], v202 offset:256
	ds_read_b64_tr_b16 v[142:143], v202 offset:2496
	s_waitcnt lgkmcnt(6)
	v_mfma_f32_16x16x32_bf16 v[66:69], v[122:125], v[144:147], v[66:69]
	ds_read_b64_tr_b16 v[144:145], v202 offset:288
	ds_read_b64_tr_b16 v[146:147], v202 offset:2528
	s_waitcnt lgkmcnt(6)
	v_mfma_f32_16x16x32_bf16 v[78:81], v[122:125], v[148:151], v[78:81]
	ds_read_b64_tr_b16 v[148:149], v202 offset:320
	ds_read_b64_tr_b16 v[150:151], v202 offset:2560
	s_waitcnt lgkmcnt(6)
	v_mfma_f32_16x16x32_bf16 v[90:93], v[122:125], v[152:155], v[90:93]
	ds_read_b64_tr_b16 v[152:153], v202 offset:352
	ds_read_b64_tr_b16 v[154:155], v202 offset:2592
	s_waitcnt lgkmcnt(6)
	v_mfma_f32_16x16x32_bf16 v[86:89], v[122:125], v[140:143], v[86:89]
	ds_read_b64_tr_b16 v[140:141], v202 offset:384
	ds_read_b64_tr_b16 v[142:143], v202 offset:2624
	s_waitcnt lgkmcnt(6)
	v_mfma_f32_16x16x32_bf16 v[82:85], v[122:125], v[144:147], v[82:85]
	ds_read_b64_tr_b16 v[144:145], v202 offset:416
	ds_read_b64_tr_b16 v[146:147], v202 offset:2656
	s_waitcnt lgkmcnt(6)
	v_mfma_f32_16x16x32_bf16 v[94:97], v[122:125], v[148:151], v[94:97]
	ds_read_b64_tr_b16 v[148:149], v202 offset:448
	ds_read_b64_tr_b16 v[150:151], v202 offset:2688
	s_waitcnt lgkmcnt(6)
	v_mfma_f32_16x16x32_bf16 v[114:117], v[122:125], v[152:155], v[114:117]
	ds_read_b64_tr_b16 v[152:153], v202 offset:480
	ds_read_b64_tr_b16 v[154:155], v202 offset:2720
	s_waitcnt lgkmcnt(6)
	v_mfma_f32_16x16x32_bf16 v[102:105], v[122:125], v[140:143], v[102:105]
	ds_read_b64_tr_b16 v[140:141], v202 offset:512
	ds_read_b64_tr_b16 v[142:143], v202 offset:2752
	s_waitcnt lgkmcnt(6)
	v_mfma_f32_16x16x32_bf16 v[106:109], v[122:125], v[144:147], v[106:109]
	s_waitcnt lgkmcnt(4)
	v_mfma_f32_16x16x32_bf16 v[98:101], v[122:125], v[148:151], v[98:101]
	s_waitcnt lgkmcnt(2)
	v_mfma_f32_16x16x32_bf16 v[110:113], v[122:125], v[152:155], v[110:113]
	s_waitcnt lgkmcnt(0)
	v_mfma_f32_16x16x32_bf16 v[118:121], v[122:125], v[140:143], v[118:121]
	s_add_i32 s70, s74, 32
	s_cmp_gt_i32 s70, s73
	s_cbranch_scc1 .LBB0_705
	s_branch .LBB0_725

.LBB0_725:
	ds_read_b64_tr_b16 v[140:141], v202 offset:17920
	ds_read_b64_tr_b16 v[142:143], v202 offset:20160
	ds_read_b64_tr_b16 v[144:145], v202 offset:17952
	ds_read_b64_tr_b16 v[146:147], v202 offset:20192
	ds_read_b64_tr_b16 v[148:149], v202 offset:17984
	ds_read_b64_tr_b16 v[150:151], v202 offset:20224
	ds_read_b128 v[122:125], v235 offset:8704
	ds_read_b128 v[136:139], v235 offset:8768
	ds_read_b128 v[132:135], v233
	v_add_u32_e32 v131, 32, v7
	v_cmp_le_i32_e32 vcc, v131, v126
	s_waitcnt lgkmcnt(2)
	v_mfma_f32_16x16x32_bf16 v[122:125], v[10:13], v[122:125], 0
	v_add_u32_e32 v7, 48, v7
	s_waitcnt lgkmcnt(1)
	v_mfma_f32_16x16x32_bf16 v[122:125], v[14:17], v[136:139], v[122:125]
	ds_read_b128 v[136:139], v233 offset:64
	s_waitcnt lgkmcnt(1)
	v_mfma_f32_16x16x32_bf16 v[132:135], v[10:13], v[132:135], 0
	s_waitcnt lgkmcnt(0)
	v_mfma_f32_16x16x32_bf16 v[132:135], v[14:17], v[136:139], v[132:135]
	ds_read_b128 v[136:139], v235 offset:8832
	s_waitcnt lgkmcnt(0)
	v_mfma_f32_16x16x32_bf16 v[122:125], v[18:21], v[136:139], v[122:125]
	ds_read_b128 v[136:139], v233 offset:128
	s_waitcnt lgkmcnt(0)
	v_mfma_f32_16x16x32_bf16 v[132:135], v[18:21], v[136:139], v[132:135]
	ds_read_b128 v[136:139], v235 offset:8896
	s_waitcnt lgkmcnt(0)
	v_mfma_f32_16x16x32_bf16 v[136:139], v[22:25], v[136:139], v[122:125]
	s_nop 2
	ds_read_b128 v[122:125], v233 offset:192
	s_waitcnt lgkmcnt(0)
	v_mfma_f32_16x16x32_bf16 v[122:125], v[22:25], v[122:125], v[132:135]
	ds_read2_b32 v[8:9], v8 offset0:32 offset1:48
	s_nop 1
	ds_read2_b32 v[132:133], v130 offset0:32 offset1:48
	s_waitcnt lgkmcnt(0)
	v_sub_f32_e32 v8, v8, v132
	v_add_f32_e32 v132, v26, v8
	v_mul_f32_e32 v132, 0x3fb8aa3b, v132
	v_exp_f32_e32 v132, v132
	s_nop 0
	v_cndmask_b32_e32 v132, 0, v132, vcc
	v_mul_f32_e32 v132, v136, v132
	v_bfe_u32 v134, v132, 16, 1
	v_add3_u32 v132, v132, v134, s14
	ds_write_b16_d16_hi v236, v132
	v_add_f32_e32 v132, v27, v8
	v_mul_f32_e32 v132, 0x3fb8aa3b, v132
	v_exp_f32_e32 v132, v132
	v_cmp_le_i32_e32 vcc, v131, v127
	s_nop 1
	v_cndmask_b32_e32 v132, 0, v132, vcc
	v_mul_f32_e32 v132, v137, v132
	v_bfe_u32 v134, v132, 16, 1
	v_add3_u32 v132, v132, v134, s14
	ds_write_b16_d16_hi v236, v132 offset:80
	v_add_f32_e32 v132, v28, v8
	v_mul_f32_e32 v132, 0x3fb8aa3b, v132
	v_add_f32_e32 v8, v29, v8
	v_exp_f32_e32 v132, v132
	v_mul_f32_e32 v8, 0x3fb8aa3b, v8
	v_exp_f32_e32 v8, v8
	v_cmp_le_i32_e32 vcc, v131, v128
	s_nop 1
	v_cndmask_b32_e32 v132, 0, v132, vcc
	v_cmp_le_i32_e32 vcc, v131, v129
	v_mul_f32_e32 v132, v138, v132
	v_bfe_u32 v134, v132, 16, 1
	v_cndmask_b32_e32 v8, 0, v8, vcc
	v_mul_f32_e32 v8, v139, v8
	v_bfe_u32 v131, v8, 16, 1
	v_add3_u32 v8, v8, v131, s14
	ds_write_b16_d16_hi v236, v8 offset:240
	v_sub_f32_e32 v8, v9, v133
	v_add_f32_e32 v9, v26, v8
	v_mul_f32_e32 v9, 0x3fb8aa3b, v9
	v_exp_f32_e32 v9, v9
	v_cmp_le_i32_e32 vcc, v7, v126
	v_add3_u32 v132, v132, v134, s14
	ds_write_b16_d16_hi v236, v132 offset:160
	v_cndmask_b32_e32 v9, 0, v9, vcc
	v_mul_f32_e32 v9, v122, v9
	v_bfe_u32 v122, v9, 16, 1
	v_add3_u32 v9, v9, v122, s14
	ds_write_b16_d16_hi v236, v9 offset:32
	v_add_f32_e32 v9, v27, v8
	v_mul_f32_e32 v9, 0x3fb8aa3b, v9
	v_exp_f32_e32 v9, v9
	v_cmp_le_i32_e32 vcc, v7, v127
	s_nop 1
	v_cndmask_b32_e32 v9, 0, v9, vcc
	v_mul_f32_e32 v9, v123, v9
	v_bfe_u32 v122, v9, 16, 1
	v_add3_u32 v9, v9, v122, s14
	ds_write_b16_d16_hi v236, v9 offset:112
	v_add_f32_e32 v9, v28, v8
	v_mul_f32_e32 v9, 0x3fb8aa3b, v9
	v_add_f32_e32 v8, v29, v8
	v_exp_f32_e32 v9, v9
	v_mul_f32_e32 v8, 0x3fb8aa3b, v8
	v_exp_f32_e32 v8, v8
	v_cmp_le_i32_e32 vcc, v7, v128
	s_nop 1
	v_cndmask_b32_e32 v9, 0, v9, vcc
	v_cmp_le_i32_e32 vcc, v7, v129
	v_mul_f32_e32 v9, v124, v9
	v_bfe_u32 v122, v9, 16, 1
	v_cndmask_b32_e32 v7, 0, v8, vcc
	v_mul_f32_e32 v7, v125, v7
	v_bfe_u32 v8, v7, 16, 1
	v_add3_u32 v9, v9, v122, s14
	v_add3_u32 v7, v7, v8, s14
	ds_write_b16_d16_hi v236, v9 offset:192
	ds_write_b16_d16_hi v236, v7 offset:272
	ds_read_b128 v[122:125], v237
	ds_read_b64_tr_b16 v[152:153], v202 offset:18016
	ds_read_b64_tr_b16 v[154:155], v202 offset:20256
	s_waitcnt lgkmcnt(2)
	v_mfma_f32_16x16x32_bf16 v[54:57], v[122:125], v[140:143], v[54:57]
	ds_read_b64_tr_b16 v[140:141], v202 offset:18048
	ds_read_b64_tr_b16 v[142:143], v202 offset:20288
	v_mfma_f32_16x16x32_bf16 v[62:65], v[122:125], v[144:147], v[62:65]
	ds_read_b64_tr_b16 v[144:145], v202 offset:18080
	ds_read_b64_tr_b16 v[146:147], v202 offset:20320
	v_mfma_f32_16x16x32_bf16 v[58:61], v[122:125], v[148:151], v[58:61]
	ds_read_b64_tr_b16 v[148:149], v202 offset:18112
	ds_read_b64_tr_b16 v[150:151], v202 offset:20352
	s_waitcnt lgkmcnt(6)
	v_mfma_f32_16x16x32_bf16 v[74:77], v[122:125], v[152:155], v[74:77]
	ds_read_b64_tr_b16 v[152:153], v202 offset:18144
	ds_read_b64_tr_b16 v[154:155], v202 offset:20384
	s_waitcnt lgkmcnt(6)
	v_mfma_f32_16x16x32_bf16 v[70:73], v[122:125], v[140:143], v[70:73]
	ds_read_b64_tr_b16 v[140:141], v202 offset:18176
	ds_read_b64_tr_b16 v[142:143], v202 offset:20416
	s_waitcnt lgkmcnt(6)
	v_mfma_f32_16x16x32_bf16 v[66:69], v[122:125], v[144:147], v[66:69]
	ds_read_b64_tr_b16 v[144:145], v202 offset:18208
	ds_read_b64_tr_b16 v[146:147], v202 offset:20448
	s_waitcnt lgkmcnt(6)
	v_mfma_f32_16x16x32_bf16 v[78:81], v[122:125], v[148:151], v[78:81]
	ds_read_b64_tr_b16 v[148:149], v202 offset:18240
	ds_read_b64_tr_b16 v[150:151], v202 offset:20480
	s_waitcnt lgkmcnt(6)
	v_mfma_f32_16x16x32_bf16 v[90:93], v[122:125], v[152:155], v[90:93]
	ds_read_b64_tr_b16 v[152:153], v202 offset:18272
	ds_read_b64_tr_b16 v[154:155], v202 offset:20512
	s_waitcnt lgkmcnt(6)
	v_mfma_f32_16x16x32_bf16 v[86:89], v[122:125], v[140:143], v[86:89]
	ds_read_b64_tr_b16 v[140:141], v202 offset:18304
	ds_read_b64_tr_b16 v[142:143], v202 offset:20544
	s_waitcnt lgkmcnt(6)
	v_mfma_f32_16x16x32_bf16 v[82:85], v[122:125], v[144:147], v[82:85]
	ds_read_b64_tr_b16 v[144:145], v202 offset:18336
	ds_read_b64_tr_b16 v[146:147], v202 offset:20576
	s_waitcnt lgkmcnt(6)
	v_mfma_f32_16x16x32_bf16 v[94:97], v[122:125], v[148:151], v[94:97]
	ds_read_b64_tr_b16 v[148:149], v202 offset:18368
	ds_read_b64_tr_b16 v[150:151], v202 offset:20608
	s_waitcnt lgkmcnt(6)
	v_mfma_f32_16x16x32_bf16 v[114:117], v[122:125], v[152:155], v[114:117]
	ds_read_b64_tr_b16 v[152:153], v202 offset:18400
	ds_read_b64_tr_b16 v[154:155], v202 offset:20640
	s_waitcnt lgkmcnt(6)
	v_mfma_f32_16x16x32_bf16 v[102:105], v[122:125], v[140:143], v[102:105]
	ds_read_b64_tr_b16 v[140:141], v202 offset:18432
	ds_read_b64_tr_b16 v[142:143], v202 offset:20672
	s_waitcnt lgkmcnt(6)
	v_mfma_f32_16x16x32_bf16 v[106:109], v[122:125], v[144:147], v[106:109]
	s_waitcnt lgkmcnt(4)
	v_mfma_f32_16x16x32_bf16 v[98:101], v[122:125], v[148:151], v[98:101]
	s_waitcnt lgkmcnt(2)
	v_mfma_f32_16x16x32_bf16 v[110:113], v[122:125], v[152:155], v[110:113]
	s_waitcnt lgkmcnt(0)
	v_mfma_f32_16x16x32_bf16 v[118:121], v[122:125], v[140:143], v[118:121]
	s_branch .LBB0_705
